# streaming nt hint on the single-use expert-output row loads of the MoE combine loop
# baseline (speedup 1.0000x reference)
; __device__ __forceinline__ u32x4 pack8(f32x4 v0, f32x4 v1) { u32x4 w; w.x = cvt_pk_bf16(v0[0], v0[1]); w.y = cvt_pk_bf16(v0[2], v0[3]); w.z = cvt_pk_bf16(v1[0], v1[1]); w.w = cvt_pk_bf16(v1[2], v1[3]); return w; }
; __device__ __forceinline__ void unpack8(u32x4 w, f32x4& v0, f32x4& v1) { v0 = (f32x4){bf_lo(w.x), bf_hi(w.x), bf_lo(w.y), bf_hi(w.y)}; v1 = (f32x4){bf_lo(w.z), bf_hi(w.z), bf_lo(w.w), bf_hi(w.w)}; }
; __global__ void __launch_bounds__(NWAVES * 64, 2) mk_fwd(Args a) {
;     ...
;             { for (int tok = gw; tok < NT; tok += ngw) { const int d0 = tokdest[tok * 2], d1 = tokdest[tok * 2 + 1]; float sq = 0.f;
; #pragma unroll
;                   for (int j = 0; j < 4; ++j) { const size_t o = (size_t)tok * DM + (lane + 64 * j) * 8; f32x4 x0, x1, p0, p1, q0, q1; epi::unpack8(*(const u32x4*)(XR + o), x0, x1);
;                       epi::unpack8(*(const u32x4*)(YB + (size_t)d0 * DM + (lane + 64 * j) * 8), p0, p1); epi::unpack8(*(const u32x4*)(YB + (size_t)d1 * DM + (lane + 64 * j) * 8), q0, q1);
;                       x0 += p0 + q0; x1 += p1 + q1;
; #pragma unroll
;                       for (int dd = 0; dd < 2; ++dd) { const int d = dd ? d1 : d0; if (d >= 16384) {
; #pragma unroll
;                           for (int s = 0; s < 3; ++s) { epi::unpack8(*(const u32x4*)((const bf16_t*)(ws + wsm::YBX) + ((size_t)s * 2048 + (d - 16384)) * DM + (lane + 64 * j) * 8), p0, p1); x0 += p0; x1 += p1; } } } *(u32x4*)(XR + o) = epi::pack8(x0, x1);
.LBB0_2412:
	s_ashr_i32 s19, s18, 31
	s_lshl_b64 s[4:5], s[18:19], 2
	s_add_u32 s4, s8, s4
	s_addc_u32 s5, s9, s5
	global_load_dwordx2 v[34:35], v3, s[4:5]
	s_waitcnt lgkmcnt(0)
	v_lshl_add_u64 v[24:25], s[52:53], 0, v[22:23]
	v_add_co_u32_e32 v36, vcc, s40, v24
	s_nop 1
	v_addc_co_u32_e32 v37, vcc, 0, v25, vcc
	global_load_dwordx4 v[26:29], v[36:37], off
	s_waitcnt vmcnt(1)
	v_readfirstlane_b32 s36, v34
	s_ashr_i32 s37, s36, 31
	v_ashrrev_i32_e32 v41, 31, v35
	v_mov_b32_e32 v40, v35
	s_lshl_b64 s[4:5], s[36:37], 12
	v_lshlrev_b64 v[40:41], 12, v[40:41]
	v_lshl_add_u64 v[38:39], v[14:15], 0, s[4:5]
	v_lshl_add_u64 v[40:41], v[14:15], 0, v[40:41]
	global_load_dwordx4 v[30:33], v[38:39], off nt
	global_load_dwordx4 v[42:45], v[40:41], off nt
	global_load_dwordx4 v[132:135], v[36:37], off offset:1024
	global_load_dwordx4 v[136:139], v[38:39], off offset:1024 nt
	global_load_dwordx4 v[140:143], v[40:41], off offset:1024 nt
	global_load_dwordx4 v[144:147], v[36:37], off offset:2048
	global_load_dwordx4 v[148:151], v[38:39], off offset:2048 nt
	global_load_dwordx4 v[152:155], v[40:41], off offset:2048 nt
	global_load_dwordx4 v[156:159], v[36:37], off offset:3072
	global_load_dwordx4 v[160:163], v[38:39], off offset:3072 nt
	global_load_dwordx4 v[164:167], v[40:41], off offset:3072 nt
	s_waitcnt vmcnt(2)
	v_lshlrev_b32_e32 v46, 16, v28
	v_and_b32_e32 v47, 0xffff0000, v28
	v_lshlrev_b32_e32 v48, 16, v29
	v_and_b32_e32 v49, 0xffff0000, v29
	v_readfirstlane_b32 s19, v35
	v_lshlrev_b32_e32 v34, 16, v26
	v_and_b32_e32 v35, 0xffff0000, v26
	v_lshlrev_b32_e32 v26, 16, v27
	v_and_b32_e32 v27, 0xffff0000, v27
	s_cmpk_gt_i32 s36, 0x3fff
	s_cselect_b64 s[6:7], -1, 0
	s_cmpk_lt_i32 s36, 0x4000
	s_waitcnt vmcnt(1)
	v_lshlrev_b32_e32 v28, 16, v30
	v_and_b32_e32 v29, 0xffff0000, v30
	v_lshlrev_b32_e32 v30, 16, v31
	v_and_b32_e32 v31, 0xffff0000, v31
	v_lshlrev_b32_e32 v50, 16, v32
	v_and_b32_e32 v51, 0xffff0000, v32
	v_lshlrev_b32_e32 v32, 16, v33
	v_and_b32_e32 v33, 0xffff0000, v33
	s_waitcnt vmcnt(0)
	v_lshlrev_b32_e32 v52, 16, v42
	v_and_b32_e32 v53, 0xffff0000, v42
	v_lshlrev_b32_e32 v42, 16, v43
	v_and_b32_e32 v43, 0xffff0000, v43
	v_lshlrev_b32_e32 v54, 16, v44
	v_and_b32_e32 v55, 0xffff0000, v44
	v_lshlrev_b32_e32 v44, 16, v45
	v_and_b32_e32 v45, 0xffff0000, v45
	v_pk_add_f32 v[28:29], v[28:29], v[52:53]
	v_pk_add_f32 v[30:31], v[30:31], v[42:43]
	v_pk_add_f32 v[42:43], v[50:51], v[54:55]
	v_pk_add_f32 v[32:33], v[32:33], v[44:45]
	v_pk_add_f32 v[26:27], v[30:31], v[26:27]
	v_pk_add_f32 v[28:29], v[28:29], v[34:35]
	v_pk_add_f32 v[30:31], v[32:33], v[48:49]
	v_pk_add_f32 v[32:33], v[42:43], v[46:47]
	s_cbranch_scc1 .LBB0_2414
	s_add_i32 s12, s36, 0xffffc000
	s_lshl_b64 s[4:5], s[12:13], 12
	v_lshl_add_u64 v[34:35], v[4:5], 0, s[4:5]
	v_add_co_u32_e32 v46, vcc, s41, v34
	global_load_dwordx4 v[42:45], v[34:35], off
	s_nop 0
	v_addc_co_u32_e32 v47, vcc, 0, v35, vcc
	global_load_dwordx4 v[46:49], v[46:47], off
	v_add_co_u32_e32 v34, vcc, s44, v34
	s_nop 1
	v_addc_co_u32_e32 v35, vcc, 0, v35, vcc
	global_load_dwordx4 v[50:53], v[34:35], off
	s_waitcnt vmcnt(2)
	v_lshlrev_b32_e32 v54, 16, v44
	v_lshlrev_b32_e32 v34, 16, v42
	v_and_b32_e32 v35, 0xffff0000, v42
	v_lshlrev_b32_e32 v42, 16, v43
	v_and_b32_e32 v43, 0xffff0000, v43
	v_and_b32_e32 v55, 0xffff0000, v44
	v_lshlrev_b32_e32 v44, 16, v45
	v_and_b32_e32 v45, 0xffff0000, v45
	v_pk_add_f32 v[26:27], v[26:27], v[42:43]
	v_pk_add_f32 v[28:29], v[28:29], v[34:35]
	v_pk_add_f32 v[30:31], v[30:31], v[44:45]
	v_pk_add_f32 v[32:33], v[32:33], v[54:55]
	s_waitcnt vmcnt(1)
	v_lshlrev_b32_e32 v34, 16, v46
	v_and_b32_e32 v35, 0xffff0000, v46
	v_lshlrev_b32_e32 v42, 16, v47
	v_and_b32_e32 v43, 0xffff0000, v47
	v_lshlrev_b32_e32 v44, 16, v48
	v_and_b32_e32 v45, 0xffff0000, v48
	v_lshlrev_b32_e32 v46, 16, v49
	v_and_b32_e32 v47, 0xffff0000, v49
	v_pk_add_f32 v[28:29], v[28:29], v[34:35]
	v_pk_add_f32 v[26:27], v[26:27], v[42:43]
	v_pk_add_f32 v[32:33], v[32:33], v[44:45]
	v_pk_add_f32 v[30:31], v[30:31], v[46:47]
	s_waitcnt vmcnt(0)
	v_lshlrev_b32_e32 v48, 16, v50
	v_and_b32_e32 v49, 0xffff0000, v50
	v_lshlrev_b32_e32 v50, 16, v51
	v_and_b32_e32 v51, 0xffff0000, v51
	v_lshlrev_b32_e32 v54, 16, v52
	v_and_b32_e32 v55, 0xffff0000, v52
	v_lshlrev_b32_e32 v52, 16, v53
	v_and_b32_e32 v53, 0xffff0000, v53
	v_pk_add_f32 v[26:27], v[26:27], v[50:51]
	v_pk_add_f32 v[28:29], v[28:29], v[48:49]
	v_pk_add_f32 v[30:31], v[30:31], v[52:53]
	v_pk_add_f32 v[32:33], v[32:33], v[54:55]
